# P6 epilogue residual-row loads prefetched (counted waits) + P8 set-up table loads batched behind one wait
# baseline (speedup 1.0000x reference)
; __device__ __forceinline__ unsigned pk2(float lo, float hi) { const f32v2 v = {lo, hi}; return __builtin_bit_cast(unsigned, __builtin_convertvector(v, bf16v2)); }
;     __device__ __forceinline__ void operator()(const f32x4 (&acc)[2][2][4][2], const pg8::Unit& u, int wr, int wc, int fr, int fq, int ui) const {
;     ...
;         const int row0 = u.pm * 256 + wr * 64 + fr, col0 = u.pn * 256 + wc * 32 + 8 * fq;
;         const float* g1 = MOD + ((u.pm * 256) / SEQ) * (6 * D) + 2 * D;
;         f32x4 gv[2][2];
; #pragma unroll
;         for (int bj = 0; bj < 2; ++bj)
; #pragma unroll
;             for (int n = 0; n < 2; ++n) gv[bj][n] = *(const f32x4*)(g1 + col0 + bj * 128 + 4 * n);
; #pragma unroll
;         for (int ai = 0; ai < 2; ++ai)
; #pragma unroll
;             for (int m = 0; m < 4; ++m) { const size_t ro = (size_t)(row0 + ai * 128 + m * 16) * D + col0;
; #pragma unroll
;                 for (int bj = 0; bj < 2; ++bj) { const u32x4 h = *(const u32x4*)(HN + ro + bj * 128); const f32x4 a0 = acc[ai][bj][m][0], a1 = acc[ai][bj][m][1], g0 = gv[bj][0], g1v = gv[bj][1];
;                     u32x4 o; o.x = pk2(ALPHA * bflo(h.x) + g0.x * a0.x, ALPHA * bfhi(h.x) + g0.y * a0.y); o.y = pk2(ALPHA * bflo(h.y) + g0.z * a0.z, ALPHA * bfhi(h.y) + g0.w * a0.w);
;                     o.z = pk2(ALPHA * bflo(h.z) + g1v.x * a1.x, ALPHA * bfhi(h.z) + g1v.y * a1.y); o.w = pk2(ALPHA * bflo(h.w) + g1v.z * a1.z, ALPHA * bfhi(h.w) + g1v.w * a1.w);
;                     *(u32x4*)(Z + ro + bj * 128) = o; } }
.LBB0_687:
	v_mov_b32_e32 v120, v223
	v_mov_b32_e32 v118, v224
	s_lshl_b32 s8, s54, 8
	s_add_i32 s8, s8, s47
	v_add_u32_e32 v120, s8, v120
	s_ashr_i32 s8, s54, 31
	s_lshr_b32 s8, s8, 28
	s_add_i32 s8, s54, s8
	s_lshl_b32 s9, s55, 8
	s_lshr_b32 s8, s8, 4
	s_or_b32 s9, s9, s48
	s_mulk_i32 s8, 0x3000
	v_lshl_add_u32 v118, v118, 3, s9
	s_ashr_i32 s9, s8, 31
	s_lshl_b64 s[8:9], s[8:9], 2
	v_ashrrev_i32_e32 v121, 31, v120
	s_add_u32 s8, s96, s8
	v_ashrrev_i32_e32 v119, 31, v118
	v_lshlrev_b64 v[120:121], 11, v[120:121]
	s_addc_u32 s9, s97, s9
	v_lshl_add_u64 v[120:121], v[120:121], 0, v[118:119]
	v_lshl_add_u64 v[122:123], v[118:119], 2, s[8:9]
	s_movk_i32 s8, 0x4000
	v_lshlrev_b64 v[146:147], 1, v[120:121]
	v_add_co_u32_e32 v118, vcc, s8, v122
	v_lshl_add_u64 v[120:121], s[12:13], 0, v[146:147]
	s_nop 0
	v_addc_co_u32_e32 v119, vcc, 0, v123, vcc
	s_mov_b64 s[8:9], 0x4000
	global_load_dwordx4 v[148:151], v[120:121], off
	global_load_dwordx4 v[152:155], v[120:121], off offset:256
	v_lshl_add_u64 v[122:123], v[122:123], 0, s[8:9]
	global_load_dwordx4 v[118:121], v[118:119], off
	s_nop 0
	global_load_dwordx4 v[126:129], v[122:123], off offset:16
	global_load_dwordx4 v[130:133], v[122:123], off offset:512
	s_nop 0
	global_load_dwordx4 v[122:125], v[122:123], off offset:528
	v_add_u32_e32 v170, 0x10000, v146
	global_load_dwordx4 v[170:173], v170, s[12:13]
	v_add_u32_e32 v174, 0x10000, v146
	global_load_dwordx4 v[174:177], v174, s[12:13] offset:256
	v_add_u32_e32 v178, 0x20000, v146
	global_load_dwordx4 v[178:181], v178, s[12:13]
	v_add_u32_e32 v182, 0x20000, v146
	global_load_dwordx4 v[182:185], v182, s[12:13] offset:256
	v_add_u32_e32 v186, 0x30000, v146
	global_load_dwordx4 v[186:189], v186, s[12:13]
	v_add_u32_e32 v190, 0x30000, v146
	global_load_dwordx4 v[190:193], v190, s[12:13] offset:256
	s_mov_b64 s[8:9], 0x10000
	v_lshl_add_u64 v[156:157], s[14:15], 0, v[146:147]
	v_lshl_add_u64 v[158:159], v[146:147], 0, s[8:9]
	s_mov_b64 s[8:9], 0x20000
	s_and_b64 vcc, exec, s[6:7]
	s_mov_b64 s[6:7], -1
	s_waitcnt vmcnt(6)
	v_lshlrev_b32_e32 v162, 16, v148
	v_and_b32_e32 v163, 0xffff0000, v148
	v_lshlrev_b32_e32 v148, 16, v149
	v_and_b32_e32 v149, 0xffff0000, v149
	v_lshlrev_b32_e32 v164, 16, v150
	v_and_b32_e32 v165, 0xffff0000, v150
	v_lshlrev_b32_e32 v150, 16, v151
	v_and_b32_e32 v151, 0xffff0000, v151
	v_pk_mul_f32 v[144:145], v[144:145], v[120:121]
	v_pk_mul_f32 v[142:143], v[142:143], v[118:119]
	v_pk_mul_f32 v[140:141], v[140:141], v[128:129]
	v_pk_mul_f32 v[138:139], v[138:139], v[126:127]
	v_lshlrev_b32_e32 v166, 16, v152
	v_and_b32_e32 v167, 0xffff0000, v152
	v_lshlrev_b32_e32 v152, 16, v153
	v_and_b32_e32 v153, 0xffff0000, v153
	v_lshlrev_b32_e32 v168, 16, v154
	v_and_b32_e32 v169, 0xffff0000, v154
	v_lshlrev_b32_e32 v154, 16, v155
	v_and_b32_e32 v155, 0xffff0000, v155
	v_pk_mul_f32 v[136:137], v[136:137], v[132:133]
	v_pk_mul_f32 v[134:135], v[134:135], v[130:131]
	v_pk_mul_f32 v[116:117], v[116:117], v[124:125]
	v_pk_mul_f32 v[114:115], v[114:115], v[122:123]
	v_pk_fma_f32 v[142:143], v[162:163], s[26:27], v[142:143] op_sel_hi:[1,0,1]
	v_pk_fma_f32 v[144:145], v[148:149], s[26:27], v[144:145] op_sel_hi:[1,0,1]
	v_pk_fma_f32 v[138:139], v[164:165], s[26:27], v[138:139] op_sel_hi:[1,0,1]
	v_pk_fma_f32 v[140:141], v[150:151], s[26:27], v[140:141] op_sel_hi:[1,0,1]
	v_pk_fma_f32 v[134:135], v[166:167], s[26:27], v[134:135] op_sel_hi:[1,0,1]
	v_pk_fma_f32 v[136:137], v[152:153], s[26:27], v[136:137] op_sel_hi:[1,0,1]
	v_pk_fma_f32 v[148:149], v[168:169], s[26:27], v[114:115] op_sel_hi:[1,0,1]
	v_pk_fma_f32 v[150:151], v[154:155], s[26:27], v[116:117] op_sel_hi:[1,0,1]
	v_cvt_pk_bf16_f32 v114, v142, v143
	v_cvt_pk_bf16_f32 v115, v144, v145
	v_cvt_pk_bf16_f32 v116, v138, v139
	v_cvt_pk_bf16_f32 v117, v140, v141
	v_cvt_pk_bf16_f32 v134, v134, v135
	v_cvt_pk_bf16_f32 v135, v136, v137
	v_cvt_pk_bf16_f32 v136, v148, v149
	v_cvt_pk_bf16_f32 v137, v150, v151
	global_store_dwordx4 v[156:157], v[114:117], off
	global_store_dwordx4 v[156:157], v[134:137], off offset:256
	v_pk_mul_f32 v[112:113], v[112:113], v[120:121]
	v_pk_mul_f32 v[110:111], v[110:111], v[118:119]
	v_pk_mul_f32 v[108:109], v[108:109], v[128:129]
	v_pk_mul_f32 v[106:107], v[106:107], v[126:127]
	v_pk_mul_f32 v[104:105], v[104:105], v[132:133]
	v_pk_mul_f32 v[102:103], v[102:103], v[130:131]
	v_pk_mul_f32 v[100:101], v[100:101], v[124:125]
	v_pk_mul_f32 v[98:99], v[98:99], v[122:123]
	v_lshl_add_u64 v[138:139], v[146:147], 0, s[8:9]
	v_lshl_add_u64 v[140:141], s[14:15], 0, v[158:159]
	v_pk_mul_f32 v[96:97], v[96:97], v[120:121]
	v_pk_mul_f32 v[94:95], v[94:95], v[118:119]
	v_pk_mul_f32 v[92:93], v[92:93], v[128:129]
	v_pk_mul_f32 v[90:91], v[90:91], v[126:127]
	s_mov_b64 s[8:9], 0x30000
	v_pk_mul_f32 v[88:89], v[88:89], v[132:133]
	v_pk_mul_f32 v[86:87], v[86:87], v[130:131]
	v_pk_mul_f32 v[84:85], v[84:85], v[124:125]
	v_pk_mul_f32 v[82:83], v[82:83], v[122:123]
	v_pk_mul_f32 v[80:81], v[80:81], v[120:121]
	v_pk_mul_f32 v[78:79], v[78:79], v[118:119]
	v_pk_mul_f32 v[76:77], v[76:77], v[128:129]
	v_pk_mul_f32 v[74:75], v[74:75], v[126:127]
	v_pk_mul_f32 v[72:73], v[72:73], v[132:133]
	v_pk_mul_f32 v[70:71], v[70:71], v[130:131]
	v_pk_mul_f32 v[68:69], v[68:69], v[124:125]
	v_pk_mul_f32 v[66:67], v[66:67], v[122:123]
	v_pk_mul_f32 v[64:65], v[64:65], v[120:121]
	v_pk_mul_f32 v[62:63], v[62:63], v[118:119]
	v_pk_mul_f32 v[60:61], v[60:61], v[128:129]
	v_pk_mul_f32 v[58:59], v[58:59], v[126:127]
	v_pk_mul_f32 v[56:57], v[56:57], v[132:133]
	v_pk_mul_f32 v[54:55], v[54:55], v[130:131]
	v_pk_mul_f32 v[52:53], v[52:53], v[124:125]
	v_pk_mul_f32 v[50:51], v[50:51], v[122:123]
	v_pk_mul_f32 v[48:49], v[48:49], v[120:121]
	v_pk_mul_f32 v[46:47], v[46:47], v[118:119]
	v_pk_mul_f32 v[44:45], v[44:45], v[128:129]
	v_pk_mul_f32 v[42:43], v[42:43], v[126:127]
	v_pk_mul_f32 v[40:41], v[40:41], v[132:133]
	v_pk_mul_f32 v[38:39], v[38:39], v[130:131]
	v_pk_mul_f32 v[36:37], v[36:37], v[124:125]
	v_pk_mul_f32 v[34:35], v[34:35], v[122:123]
	v_pk_mul_f32 v[32:33], v[32:33], v[120:121]
	v_pk_mul_f32 v[30:31], v[30:31], v[118:119]
	v_pk_mul_f32 v[28:29], v[28:29], v[128:129]
	v_pk_mul_f32 v[26:27], v[26:27], v[126:127]
	v_pk_mul_f32 v[24:25], v[24:25], v[132:133]
	v_pk_mul_f32 v[22:23], v[22:23], v[130:131]
	v_pk_mul_f32 v[20:21], v[20:21], v[124:125]
	v_pk_mul_f32 v[18:19], v[18:19], v[122:123]
	v_pk_mul_f32 v[16:17], v[16:17], v[120:121]
	v_pk_mul_f32 v[14:15], v[14:15], v[118:119]
	v_pk_mul_f32 v[12:13], v[12:13], v[128:129]
	v_pk_mul_f32 v[10:11], v[10:11], v[126:127]
	v_pk_mul_f32 v[8:9], v[8:9], v[132:133]
	v_pk_mul_f32 v[6:7], v[6:7], v[130:131]
	v_pk_mul_f32 v[4:5], v[4:5], v[124:125]
	v_pk_mul_f32 v[2:3], v[2:3], v[122:123]
	s_waitcnt vmcnt(6)
; __device__ __forceinline__ unsigned pk2(float lo, float hi) { const f32v2 v = {lo, hi}; return __builtin_bit_cast(unsigned, __builtin_convertvector(v, bf16v2)); }
;     __device__ __forceinline__ void operator()(const f32x4 (&acc)[2][2][4][2], const pg8::Unit& u, int wr, int wc, int fr, int fq, int ui) const {
;     ...
;         for (int ai = 0; ai < 2; ++ai)
; #pragma unroll
;             for (int m = 0; m < 4; ++m) { const size_t ro = (size_t)(row0 + ai * 128 + m * 16) * D + col0;
; #pragma unroll
;                 for (int bj = 0; bj < 2; ++bj) { const u32x4 h = *(const u32x4*)(HN + ro + bj * 128); const f32x4 a0 = acc[ai][bj][m][0], a1 = acc[ai][bj][m][1], g0 = gv[bj][0], g1v = gv[bj][1];
;                     u32x4 o; o.x = pk2(ALPHA * bflo(h.x) + g0.x * a0.x, ALPHA * bfhi(h.x) + g0.y * a0.y); o.y = pk2(ALPHA * bflo(h.y) + g0.z * a0.z, ALPHA * bfhi(h.y) + g0.w * a0.w);
;                     o.z = pk2(ALPHA * bflo(h.z) + g1v.x * a1.x, ALPHA * bfhi(h.z) + g1v.y * a1.y); o.w = pk2(ALPHA * bflo(h.w) + g1v.z * a1.z, ALPHA * bfhi(h.w) + g1v.w * a1.w);
;                     *(u32x4*)(Z + ro + bj * 128) = o; } }
	v_lshlrev_b32_e32 v144, 16, v170
	v_and_b32_e32 v145, 0xffff0000, v170
	v_lshlrev_b32_e32 v114, 16, v171
	v_and_b32_e32 v115, 0xffff0000, v171
	v_lshlrev_b32_e32 v148, 16, v172
	v_and_b32_e32 v149, 0xffff0000, v172
	v_lshlrev_b32_e32 v116, 16, v173
	v_and_b32_e32 v117, 0xffff0000, v173
	v_lshlrev_b32_e32 v150, 16, v174
	v_and_b32_e32 v151, 0xffff0000, v174
	v_lshlrev_b32_e32 v134, 16, v175
	v_and_b32_e32 v135, 0xffff0000, v175
	v_lshlrev_b32_e32 v152, 16, v176
	v_and_b32_e32 v153, 0xffff0000, v176
	v_lshlrev_b32_e32 v136, 16, v177
	v_and_b32_e32 v137, 0xffff0000, v177
	v_pk_fma_f32 v[110:111], v[144:145], s[26:27], v[110:111] op_sel_hi:[1,0,1]
	v_pk_fma_f32 v[112:113], v[114:115], s[26:27], v[112:113] op_sel_hi:[1,0,1]
	v_pk_fma_f32 v[106:107], v[148:149], s[26:27], v[106:107] op_sel_hi:[1,0,1]
	v_pk_fma_f32 v[108:109], v[116:117], s[26:27], v[108:109] op_sel_hi:[1,0,1]
	v_pk_fma_f32 v[102:103], v[150:151], s[26:27], v[102:103] op_sel_hi:[1,0,1]
	v_pk_fma_f32 v[104:105], v[134:135], s[26:27], v[104:105] op_sel_hi:[1,0,1]
	v_pk_fma_f32 v[114:115], v[152:153], s[26:27], v[98:99] op_sel_hi:[1,0,1]
	v_pk_fma_f32 v[116:117], v[136:137], s[26:27], v[100:101] op_sel_hi:[1,0,1]
	v_cvt_pk_bf16_f32 v98, v110, v111
	v_cvt_pk_bf16_f32 v99, v112, v113
	v_cvt_pk_bf16_f32 v100, v106, v107
	v_cvt_pk_bf16_f32 v101, v108, v109
	v_cvt_pk_bf16_f32 v102, v102, v103
	v_cvt_pk_bf16_f32 v103, v104, v105
	v_cvt_pk_bf16_f32 v104, v114, v115
	v_cvt_pk_bf16_f32 v105, v116, v117
	global_store_dwordx4 v[140:141], v[98:101], off
	global_store_dwordx4 v[140:141], v[102:105], off offset:256
	v_add_u32_e32 v170, 0x80000, v146
	global_load_dwordx4 v[170:173], v170, s[12:13]
	v_add_u32_e32 v174, 0x80000, v146
	global_load_dwordx4 v[174:177], v174, s[12:13] offset:256
	v_lshl_add_u64 v[106:107], v[146:147], 0, s[8:9]
	v_lshl_add_u64 v[108:109], s[14:15], 0, v[138:139]
	s_mov_b64 s[8:9], 0x80000
	s_waitcnt vmcnt(8)
	v_lshlrev_b32_e32 v112, 16, v178
	v_and_b32_e32 v113, 0xffff0000, v178
	v_lshlrev_b32_e32 v98, 16, v179
	v_and_b32_e32 v99, 0xffff0000, v179
	v_lshlrev_b32_e32 v114, 16, v180
	v_and_b32_e32 v115, 0xffff0000, v180
	v_lshlrev_b32_e32 v100, 16, v181
	v_and_b32_e32 v101, 0xffff0000, v181
	v_lshlrev_b32_e32 v116, 16, v182
	v_and_b32_e32 v117, 0xffff0000, v182
	v_lshlrev_b32_e32 v102, 16, v183
	v_and_b32_e32 v103, 0xffff0000, v183
	v_lshlrev_b32_e32 v134, 16, v184
	v_and_b32_e32 v135, 0xffff0000, v184
	v_lshlrev_b32_e32 v104, 16, v185
	v_and_b32_e32 v105, 0xffff0000, v185
	v_pk_fma_f32 v[94:95], v[112:113], s[26:27], v[94:95] op_sel_hi:[1,0,1]
	v_pk_fma_f32 v[96:97], v[98:99], s[26:27], v[96:97] op_sel_hi:[1,0,1]
	v_pk_fma_f32 v[90:91], v[114:115], s[26:27], v[90:91] op_sel_hi:[1,0,1]
	v_pk_fma_f32 v[92:93], v[100:101], s[26:27], v[92:93] op_sel_hi:[1,0,1]
	v_pk_fma_f32 v[86:87], v[116:117], s[26:27], v[86:87] op_sel_hi:[1,0,1]
	v_pk_fma_f32 v[88:89], v[102:103], s[26:27], v[88:89] op_sel_hi:[1,0,1]
	v_pk_fma_f32 v[98:99], v[134:135], s[26:27], v[82:83] op_sel_hi:[1,0,1]
	v_pk_fma_f32 v[100:101], v[104:105], s[26:27], v[84:85] op_sel_hi:[1,0,1]
	v_cvt_pk_bf16_f32 v82, v94, v95
	v_cvt_pk_bf16_f32 v83, v96, v97
	v_cvt_pk_bf16_f32 v84, v90, v91
	v_cvt_pk_bf16_f32 v85, v92, v93
	v_cvt_pk_bf16_f32 v86, v86, v87
	v_cvt_pk_bf16_f32 v87, v88, v89
	v_cvt_pk_bf16_f32 v88, v98, v99
	v_cvt_pk_bf16_f32 v89, v100, v101
	global_store_dwordx4 v[108:109], v[82:85], off
	global_store_dwordx4 v[108:109], v[86:89], off offset:256
	v_add_u32_e32 v178, 0x90000, v146
	global_load_dwordx4 v[178:181], v178, s[12:13]
	v_add_u32_e32 v182, 0x90000, v146
	global_load_dwordx4 v[182:185], v182, s[12:13] offset:256
	v_lshl_add_u64 v[90:91], v[146:147], 0, s[8:9]
	v_lshl_add_u64 v[92:93], s[14:15], 0, v[106:107]
	s_mov_b64 s[8:9], 0x90000
	s_waitcnt vmcnt(10)
	v_lshlrev_b32_e32 v96, 16, v186
	v_and_b32_e32 v97, 0xffff0000, v186
	v_lshlrev_b32_e32 v82, 16, v187
	v_and_b32_e32 v83, 0xffff0000, v187
	v_lshlrev_b32_e32 v98, 16, v188
	v_and_b32_e32 v99, 0xffff0000, v188
	v_lshlrev_b32_e32 v84, 16, v189
	v_and_b32_e32 v85, 0xffff0000, v189
	v_lshlrev_b32_e32 v100, 16, v190
	v_and_b32_e32 v101, 0xffff0000, v190
	v_lshlrev_b32_e32 v86, 16, v191
	v_and_b32_e32 v87, 0xffff0000, v191
	v_lshlrev_b32_e32 v102, 16, v192
	v_and_b32_e32 v103, 0xffff0000, v192
	v_lshlrev_b32_e32 v88, 16, v193
	v_and_b32_e32 v89, 0xffff0000, v193
	v_pk_fma_f32 v[78:79], v[96:97], s[26:27], v[78:79] op_sel_hi:[1,0,1]
	v_pk_fma_f32 v[80:81], v[82:83], s[26:27], v[80:81] op_sel_hi:[1,0,1]
	v_pk_fma_f32 v[74:75], v[98:99], s[26:27], v[74:75] op_sel_hi:[1,0,1]
	v_pk_fma_f32 v[76:77], v[84:85], s[26:27], v[76:77] op_sel_hi:[1,0,1]
	v_pk_fma_f32 v[70:71], v[100:101], s[26:27], v[70:71] op_sel_hi:[1,0,1]
	v_pk_fma_f32 v[72:73], v[86:87], s[26:27], v[72:73] op_sel_hi:[1,0,1]
	v_pk_fma_f32 v[82:83], v[102:103], s[26:27], v[66:67] op_sel_hi:[1,0,1]
	v_pk_fma_f32 v[84:85], v[88:89], s[26:27], v[68:69] op_sel_hi:[1,0,1]
	v_cvt_pk_bf16_f32 v66, v78, v79
	v_cvt_pk_bf16_f32 v67, v80, v81
	v_cvt_pk_bf16_f32 v68, v74, v75
	v_cvt_pk_bf16_f32 v69, v76, v77
	v_cvt_pk_bf16_f32 v70, v70, v71
	v_cvt_pk_bf16_f32 v71, v72, v73
	v_cvt_pk_bf16_f32 v72, v82, v83
	v_cvt_pk_bf16_f32 v73, v84, v85
	global_store_dwordx4 v[92:93], v[66:69], off
	global_store_dwordx4 v[92:93], v[70:73], off offset:256
	v_add_u32_e32 v186, 0xa0000, v146
	global_load_dwordx4 v[186:189], v186, s[12:13]
	v_add_u32_e32 v190, 0xa0000, v146
	global_load_dwordx4 v[190:193], v190, s[12:13] offset:256
	v_lshl_add_u64 v[74:75], v[146:147], 0, s[8:9]
	v_lshl_add_u64 v[76:77], s[14:15], 0, v[90:91]
	s_mov_b64 s[8:9], 0xa0000
	s_waitcnt vmcnt(8)
; __device__ __forceinline__ unsigned pk2(float lo, float hi) { const f32v2 v = {lo, hi}; return __builtin_bit_cast(unsigned, __builtin_convertvector(v, bf16v2)); }
;     __device__ __forceinline__ void operator()(const f32x4 (&acc)[2][2][4][2], const pg8::Unit& u, int wr, int wc, int fr, int fq, int ui) const {
;     ...
;         for (int ai = 0; ai < 2; ++ai)
; #pragma unroll
;             for (int m = 0; m < 4; ++m) { const size_t ro = (size_t)(row0 + ai * 128 + m * 16) * D + col0;
; #pragma unroll
;                 for (int bj = 0; bj < 2; ++bj) { const u32x4 h = *(const u32x4*)(HN + ro + bj * 128); const f32x4 a0 = acc[ai][bj][m][0], a1 = acc[ai][bj][m][1], g0 = gv[bj][0], g1v = gv[bj][1];
;                     u32x4 o; o.x = pk2(ALPHA * bflo(h.x) + g0.x * a0.x, ALPHA * bfhi(h.x) + g0.y * a0.y); o.y = pk2(ALPHA * bflo(h.y) + g0.z * a0.z, ALPHA * bfhi(h.y) + g0.w * a0.w);
;                     o.z = pk2(ALPHA * bflo(h.z) + g1v.x * a1.x, ALPHA * bfhi(h.z) + g1v.y * a1.y); o.w = pk2(ALPHA * bflo(h.w) + g1v.z * a1.z, ALPHA * bfhi(h.w) + g1v.w * a1.w);
;                     *(u32x4*)(Z + ro + bj * 128) = o; } }
	v_lshlrev_b32_e32 v80, 16, v170
	v_and_b32_e32 v81, 0xffff0000, v170
	v_lshlrev_b32_e32 v66, 16, v171
	v_and_b32_e32 v67, 0xffff0000, v171
	v_lshlrev_b32_e32 v82, 16, v172
	v_and_b32_e32 v83, 0xffff0000, v172
	v_lshlrev_b32_e32 v68, 16, v173
	v_and_b32_e32 v69, 0xffff0000, v173
	v_lshlrev_b32_e32 v84, 16, v174
	v_and_b32_e32 v85, 0xffff0000, v174
	v_lshlrev_b32_e32 v70, 16, v175
	v_and_b32_e32 v71, 0xffff0000, v175
	v_lshlrev_b32_e32 v86, 16, v176
	v_and_b32_e32 v87, 0xffff0000, v176
	v_lshlrev_b32_e32 v72, 16, v177
	v_and_b32_e32 v73, 0xffff0000, v177
	v_pk_fma_f32 v[62:63], v[80:81], s[26:27], v[62:63] op_sel_hi:[1,0,1]
	v_pk_fma_f32 v[64:65], v[66:67], s[26:27], v[64:65] op_sel_hi:[1,0,1]
	v_pk_fma_f32 v[58:59], v[82:83], s[26:27], v[58:59] op_sel_hi:[1,0,1]
	v_pk_fma_f32 v[60:61], v[68:69], s[26:27], v[60:61] op_sel_hi:[1,0,1]
	v_pk_fma_f32 v[54:55], v[84:85], s[26:27], v[54:55] op_sel_hi:[1,0,1]
	v_pk_fma_f32 v[56:57], v[70:71], s[26:27], v[56:57] op_sel_hi:[1,0,1]
	v_pk_fma_f32 v[66:67], v[86:87], s[26:27], v[50:51] op_sel_hi:[1,0,1]
	v_pk_fma_f32 v[68:69], v[72:73], s[26:27], v[52:53] op_sel_hi:[1,0,1]
	v_cvt_pk_bf16_f32 v50, v62, v63
	v_cvt_pk_bf16_f32 v51, v64, v65
	v_cvt_pk_bf16_f32 v52, v58, v59
	v_cvt_pk_bf16_f32 v53, v60, v61
	v_cvt_pk_bf16_f32 v54, v54, v55
	v_cvt_pk_bf16_f32 v55, v56, v57
	v_cvt_pk_bf16_f32 v56, v66, v67
	v_cvt_pk_bf16_f32 v57, v68, v69
	global_store_dwordx4 v[76:77], v[50:53], off
	global_store_dwordx4 v[76:77], v[54:57], off offset:256
	v_add_u32_e32 v170, 0xb0000, v146
	global_load_dwordx4 v[170:173], v170, s[12:13]
	v_add_u32_e32 v174, 0xb0000, v146
	global_load_dwordx4 v[174:177], v174, s[12:13] offset:256
	v_lshl_add_u64 v[58:59], v[146:147], 0, s[8:9]
	v_lshl_add_u64 v[60:61], s[14:15], 0, v[74:75]
	s_mov_b64 s[8:9], 0xb0000
	s_waitcnt vmcnt(8)
	v_lshlrev_b32_e32 v64, 16, v178
	v_and_b32_e32 v65, 0xffff0000, v178
	v_lshlrev_b32_e32 v50, 16, v179
	v_and_b32_e32 v51, 0xffff0000, v179
	v_lshlrev_b32_e32 v66, 16, v180
	v_and_b32_e32 v67, 0xffff0000, v180
	v_lshlrev_b32_e32 v52, 16, v181
	v_and_b32_e32 v53, 0xffff0000, v181
	v_lshlrev_b32_e32 v68, 16, v182
	v_and_b32_e32 v69, 0xffff0000, v182
	v_lshlrev_b32_e32 v54, 16, v183
	v_and_b32_e32 v55, 0xffff0000, v183
	v_lshlrev_b32_e32 v70, 16, v184
	v_and_b32_e32 v71, 0xffff0000, v184
	v_lshlrev_b32_e32 v56, 16, v185
	v_and_b32_e32 v57, 0xffff0000, v185
	v_pk_fma_f32 v[46:47], v[64:65], s[26:27], v[46:47] op_sel_hi:[1,0,1]
	v_pk_fma_f32 v[48:49], v[50:51], s[26:27], v[48:49] op_sel_hi:[1,0,1]
	v_pk_fma_f32 v[42:43], v[66:67], s[26:27], v[42:43] op_sel_hi:[1,0,1]
	v_pk_fma_f32 v[44:45], v[52:53], s[26:27], v[44:45] op_sel_hi:[1,0,1]
	v_pk_fma_f32 v[38:39], v[68:69], s[26:27], v[38:39] op_sel_hi:[1,0,1]
	v_pk_fma_f32 v[40:41], v[54:55], s[26:27], v[40:41] op_sel_hi:[1,0,1]
	v_pk_fma_f32 v[50:51], v[70:71], s[26:27], v[34:35] op_sel_hi:[1,0,1]
	v_pk_fma_f32 v[52:53], v[56:57], s[26:27], v[36:37] op_sel_hi:[1,0,1]
	v_cvt_pk_bf16_f32 v34, v46, v47
	v_cvt_pk_bf16_f32 v35, v48, v49
	v_cvt_pk_bf16_f32 v36, v42, v43
	v_cvt_pk_bf16_f32 v37, v44, v45
	v_cvt_pk_bf16_f32 v38, v38, v39
	v_cvt_pk_bf16_f32 v39, v40, v41
	v_cvt_pk_bf16_f32 v40, v50, v51
	v_cvt_pk_bf16_f32 v41, v52, v53
	global_store_dwordx4 v[60:61], v[34:37], off
	global_store_dwordx4 v[60:61], v[38:41], off offset:256
	v_lshl_add_u64 v[42:43], v[146:147], 0, s[8:9]
	v_lshl_add_u64 v[44:45], s[14:15], 0, v[58:59]
	s_waitcnt vmcnt(6)
	v_lshlrev_b32_e32 v48, 16, v186
	v_and_b32_e32 v49, 0xffff0000, v186
	v_lshlrev_b32_e32 v34, 16, v187
	v_and_b32_e32 v35, 0xffff0000, v187
	v_lshlrev_b32_e32 v50, 16, v188
	v_and_b32_e32 v51, 0xffff0000, v188
	v_lshlrev_b32_e32 v36, 16, v189
	v_and_b32_e32 v37, 0xffff0000, v189
	v_lshlrev_b32_e32 v52, 16, v190
	v_and_b32_e32 v53, 0xffff0000, v190
	v_lshlrev_b32_e32 v38, 16, v191
	v_and_b32_e32 v39, 0xffff0000, v191
	v_lshlrev_b32_e32 v54, 16, v192
	v_and_b32_e32 v55, 0xffff0000, v192
	v_lshlrev_b32_e32 v40, 16, v193
	v_and_b32_e32 v41, 0xffff0000, v193
	v_pk_fma_f32 v[30:31], v[48:49], s[26:27], v[30:31] op_sel_hi:[1,0,1]
	v_pk_fma_f32 v[32:33], v[34:35], s[26:27], v[32:33] op_sel_hi:[1,0,1]
	v_pk_fma_f32 v[26:27], v[50:51], s[26:27], v[26:27] op_sel_hi:[1,0,1]
	v_pk_fma_f32 v[28:29], v[36:37], s[26:27], v[28:29] op_sel_hi:[1,0,1]
	v_pk_fma_f32 v[22:23], v[52:53], s[26:27], v[22:23] op_sel_hi:[1,0,1]
	v_pk_fma_f32 v[24:25], v[38:39], s[26:27], v[24:25] op_sel_hi:[1,0,1]
	v_pk_fma_f32 v[34:35], v[54:55], s[26:27], v[18:19] op_sel_hi:[1,0,1]
	v_pk_fma_f32 v[36:37], v[40:41], s[26:27], v[20:21] op_sel_hi:[1,0,1]
	v_cvt_pk_bf16_f32 v18, v30, v31
	v_cvt_pk_bf16_f32 v19, v32, v33
	v_cvt_pk_bf16_f32 v20, v26, v27
	v_cvt_pk_bf16_f32 v21, v28, v29
	v_cvt_pk_bf16_f32 v22, v22, v23
	v_cvt_pk_bf16_f32 v23, v24, v25
	v_cvt_pk_bf16_f32 v24, v34, v35
	v_cvt_pk_bf16_f32 v25, v36, v37
	global_store_dwordx4 v[44:45], v[18:21], off
	global_store_dwordx4 v[44:45], v[22:25], off offset:256
	v_lshl_add_u64 v[26:27], s[14:15], 0, v[42:43]
	s_waitcnt vmcnt(4)
	v_lshlrev_b32_e32 v28, 16, v170
	v_and_b32_e32 v29, 0xffff0000, v170
	v_lshlrev_b32_e32 v18, 16, v171
	v_and_b32_e32 v19, 0xffff0000, v171
	v_lshlrev_b32_e32 v30, 16, v172
	v_and_b32_e32 v31, 0xffff0000, v172
	v_lshlrev_b32_e32 v20, 16, v173
	v_and_b32_e32 v21, 0xffff0000, v173
	v_lshlrev_b32_e32 v32, 16, v174
	v_and_b32_e32 v33, 0xffff0000, v174
	v_lshlrev_b32_e32 v22, 16, v175
	v_and_b32_e32 v23, 0xffff0000, v175
	v_lshlrev_b32_e32 v34, 16, v176
	v_and_b32_e32 v35, 0xffff0000, v176
	v_lshlrev_b32_e32 v24, 16, v177
	v_and_b32_e32 v25, 0xffff0000, v177
	v_pk_fma_f32 v[14:15], v[28:29], s[26:27], v[14:15] op_sel_hi:[1,0,1]
	v_pk_fma_f32 v[16:17], v[18:19], s[26:27], v[16:17] op_sel_hi:[1,0,1]
	v_pk_fma_f32 v[10:11], v[30:31], s[26:27], v[10:11] op_sel_hi:[1,0,1]
	v_pk_fma_f32 v[12:13], v[20:21], s[26:27], v[12:13] op_sel_hi:[1,0,1]
	v_pk_fma_f32 v[6:7], v[32:33], s[26:27], v[6:7] op_sel_hi:[1,0,1]
	v_pk_fma_f32 v[8:9], v[22:23], s[26:27], v[8:9] op_sel_hi:[1,0,1]
	v_pk_fma_f32 v[18:19], v[34:35], s[26:27], v[2:3] op_sel_hi:[1,0,1]
	v_pk_fma_f32 v[20:21], v[24:25], s[26:27], v[4:5] op_sel_hi:[1,0,1]
	v_cvt_pk_bf16_f32 v2, v14, v15
	v_cvt_pk_bf16_f32 v3, v16, v17
	v_cvt_pk_bf16_f32 v4, v10, v11
	v_cvt_pk_bf16_f32 v5, v12, v13
	v_cvt_pk_bf16_f32 v6, v6, v7
	v_cvt_pk_bf16_f32 v7, v8, v9
	v_cvt_pk_bf16_f32 v8, v18, v19
	v_cvt_pk_bf16_f32 v9, v20, v21
	global_store_dwordx4 v[26:27], v[2:5], off
	global_store_dwordx4 v[26:27], v[6:9], off offset:256
	s_cbranch_vccnz .LBB0_671
	s_andn2_b64 vcc, exec, s[10:11]
	s_cbranch_vccnz .LBB0_670
	s_barrier
	s_branch .LBB0_670
